# retention unit: the four group-norm weight row loads hoisted out of the chunk loop; on top of v26
# baseline (speedup 1.0000x reference)
.LBB0_834:
	s_or_b64 exec, exec, s[12:13]
	v_cvt_f32_i32_e32 v2, s1
	s_mov_b32 s16, 0xc2fc0000
	v_mov_b32_e32 v44, 0x42800000
	v_bfe_u32 v102, v0, 1, 7
	v_sub_f32_e32 v2, 0xc0a00000, v2
	v_cmp_gt_f32_e32 vcc, s16, v2
	s_and_b64 s[12:13], vcc, exec
	s_cselect_b32 s12, 0xffffffc0, 0
	v_cndmask_b32_e32 v3, 0, v44, vcc
	v_add_f32_e32 v2, v2, v3
	v_exp_f32_e32 v2, v2
	v_cmp_gt_i32_e64 s[26:27], s87, v0
	v_ashrrev_i32_e32 v103, 2, v0
	v_and_b32_e32 v31, 1, v26
	v_ldexp_f32 v2, v2, s12
	v_sub_f32_e32 v62, 1.0, v2
	s_mov_b32 s12, 0x800000
	v_cmp_gt_f32_e32 vcc, s12, v62
	s_and_b64 s[12:13], vcc, exec
	s_cselect_b32 s12, 32, 0
	v_ldexp_f32 v3, v62, s12
	v_log_f32_e32 v3, v3
	v_mov_b32_e32 v2, 0x42000000
	v_cndmask_b32_e32 v2, 0, v2, vcc
	v_mov_b64_e32 v[18:19], s[74:75]
	v_sub_f32_e32 v30, v3, v2
	v_mul_f32_e32 v2, 0x42fe0000, v30
	v_cmp_gt_f32_e32 vcc, s16, v2
	s_and_b64 s[12:13], vcc, exec
	s_cselect_b32 s12, 0xffffffc0, 0
	v_cndmask_b32_e32 v2, 0, v44, vcc
	v_fmac_f32_e32 v2, 0x42fe0000, v30
	v_exp_f32_e32 v2, v2
	s_lshl_b32 s68, s1, 6
	s_ashr_i32 s69, s68, 31
	s_lshl_b32 s18, s0, 12
	v_ldexp_f32 v66, v2, s12
	s_movk_i32 s12, 0xff
	v_cmp_lt_i32_e32 vcc, s12, v0
	v_mov_b32_e32 v0, 0x500
	v_mov_b32_e32 v2, 0x600
	v_cndmask_b32_e32 v0, v0, v2, vcc
	v_lshl_add_u64 v[2:3], v[0:1], 0, s[68:69]
	v_or_b32_e32 v0, s18, v102
	v_lshl_or_b32 v2, v31, 4, v2
	v_mad_i64_i32 v[4:5], s[12:13], v0, s2, v[18:19]
	v_add_u32_e32 v0, s18, v103
	v_lshlrev_b64 v[28:29], 1, v[2:3]
	v_mad_i64_i32 v[18:19], s[12:13], v0, s2, v[18:19]
	v_lshl_add_u64 v[14:15], v[4:5], 0, v[28:29]
	s_lshl_b64 s[12:13], s[68:69], 1
	v_lshlrev_b32_e32 v0, 5, v26
	global_load_dwordx4 v[2:5], v[14:15], off offset:16
	global_load_dwordx4 v[6:9], v[14:15], off
	global_load_dwordx4 v[10:13], v[14:15], off offset:80
	s_nop 0
	global_load_dwordx4 v[14:17], v[14:15], off offset:64
	v_lshl_add_u64 v[18:19], v[18:19], 0, s[12:13]
	v_and_b32_e32 v0, 0x60, v0
	v_lshl_add_u64 v[22:23], v[18:19], 0, v[0:1]
	global_load_dwordx4 v[18:21], v[22:23], off offset:3600
	s_nop 0
	global_load_dwordx4 v[22:25], v[22:23], off offset:3584
	v_lshlrev_b32_e32 v32, 4, v103
	s_ashr_i32 s1, s0, 31
	v_and_b32_e32 v32, 0x60, v32
	v_or_b32_e32 v34, 16, v0
	s_lshl_b64 s[0:1], s[0:1], 12
	v_and_b32_e32 v27, 15, v26
	v_xad_u32 v33, v32, v0, 0
	v_xad_u32 v32, v32, v34, 0
	v_lshl_add_u64 v[70:71], s[74:75], 0, v[28:29]
	s_add_u32 s0, s0, s92
	v_ashrrev_i32_e32 v28, 2, v26
	v_and_b32_e32 v34, -16, v26
	v_lshlrev_b32_e32 v35, 4, v26
	v_bfe_u32 v36, v26, 2, 2
	v_lshlrev_b32_e32 v26, 3, v26
	v_or_b32_e32 v72, s0, v27
	v_and_b32_e32 v26, 24, v26
	v_readlane_b32 s0, v252, 44
	v_cvt_f32_ubyte0_e32 v41, v102
	s_addc_u32 s1, s1, 0
	v_and_b32_e32 v74, -4, v28
	v_or_b32_e32 v38, s0, v26
	v_readlane_b32 s0, v252, 45
	v_mul_f32_e32 v42, v30, v41
	v_mov_b32_e32 v73, s1
	v_add_u32_e32 v39, s0, v74
	v_cmp_gt_f32_e64 s[0:1], s16, v42
	v_mul_f32_e64 v43, v30, -v41
	v_cmp_gt_f32_e64 s[28:29], s16, v43
	v_cndmask_b32_e64 v42, 0, v44, s[0:1]
	v_fmac_f32_e32 v42, v30, v41
	v_cndmask_b32_e64 v43, 0, v44, s[28:29]
	v_exp_f32_e32 v42, v42
	v_fma_f32 v30, v30, -v41, v43
	v_exp_f32_e32 v30, v30
	v_not_b32_e32 v43, 63
	v_cndmask_b32_e64 v41, 0, v43, s[0:1]
	s_add_i32 s41, 0, 0x10000
	v_ldexp_f32 v41, v42, v41
	v_cndmask_b32_e64 v42, 0, v43, s[28:29]
	s_lshl_b64 s[0:1], s[68:69], 2
	v_readlane_b32 s16, v254, 53
	v_ldexp_f32 v30, v30, v42
	s_add_u32 s0, s16, s0
	v_readlane_b32 s16, v254, 54
	v_ashrrev_i32_e32 v75, 31, v74
	v_mul_f32_e32 v30, 0x3e000000, v30
	s_addc_u32 s1, s16, s1
	v_lshl_add_u64 v[80:81], v[74:75], 2, s[0:1]
	v_cndmask_b32_e32 v82, v41, v30, vcc
	s_movk_i32 s0, 0x70
	v_add_u32_e32 v30, 64, v34
	v_lshlrev_b32_e32 v40, 1, v27
	v_bitop3_b32 v107, v35, v34, s0 bitop3:0x6c
	v_bitop3_b32 v108, v35, v30, s0 bitop3:0x6c
	v_readlane_b32 s0, v252, 46
	v_lshlrev_b32_e32 v104, 5, v31
	v_lshlrev_b32_e32 v43, 4, v102
	v_or_b32_e32 v52, s0, v26
	v_or_b32_e32 v53, s95, v40
	v_or_b32_e32 v40, s0, v40
	s_add_u32 s0, s74, s12
	v_or_b32_e32 v37, v74, v36
	v_and_b32_e32 v44, 0x70, v43
	v_or_b32_e32 v46, 16, v104
	v_or_b32_e32 v48, 64, v104
	v_or_b32_e32 v50, 0x50, v104
	v_and_b32_e32 v43, 0x60, v43
	v_lshlrev_b32_e32 v54, 7, v39
	v_or_b32_e32 v57, 1, v39
	v_or_b32_e32 v60, 2, v39
	v_or_b32_e32 v39, 3, v39
	s_addc_u32 s1, s75, s13
	v_or_b32_e32 v29, s92, v27
	v_xad_u32 v45, v44, v104, 0
	v_xad_u32 v47, v44, v46, 0
	v_xad_u32 v49, v44, v48, 0
	v_xad_u32 v44, v44, v50, 0
	v_xad_u32 v51, v43, v104, 0
	v_xad_u32 v46, v43, v46, 0
	v_xad_u32 v48, v43, v48, 0
	v_xad_u32 v43, v43, v50, 0
	v_sub_u32_e32 v50, v27, v74
	v_lshlrev_b32_e32 v34, 4, v37
	v_lshlrev_b32_e32 v55, 4, v28
	v_lshlrev_b32_e32 v58, 7, v57
	v_lshlrev_b32_e32 v57, 4, v57
	v_lshlrev_b32_e32 v61, 7, v60
	v_lshlrev_b32_e32 v60, 4, v60
	v_lshlrev_b32_e32 v67, 7, v39
	v_lshlrev_b32_e32 v39, 4, v39
	v_lshl_add_u64 v[84:85], s[0:1], 0, v[0:1]
	v_lshrrev_b32_e32 v0, 2, v28
	v_lshlrev_b32_e32 v28, 7, v36
	v_lshl_add_u32 v105, v29, 7, 0
	v_lshlrev_b32_e32 v29, 7, v27
	v_lshlrev_b32_e32 v30, 7, v37
	v_and_b32_e32 v35, 0x60, v34
	v_cmp_lt_i32_e64 s[28:29], -1, v50
	v_cmp_lt_i32_e64 s[30:31], 0, v50
	v_cmp_lt_i32_e64 s[34:35], 1, v50
	v_cmp_lt_i32_e64 s[36:37], 2, v50
	v_or_b32_e32 v37, 32, v26
	s_movk_i32 s16, 0x60
	v_or_b32_e32 v41, 64, v26
	v_or_b32_e32 v50, s95, v26
	v_and_b32_e32 v55, 64, v55
	v_and_b32_e32 v57, 0x50, v57
	v_and_b32_e32 v60, 0x60, v60
	v_and_b32_e32 v39, 0x70, v39
	v_lshl_or_b32 v28, v0, 9, v28
	v_lshlrev_b32_e32 v0, 6, v0
	v_lshlrev_b32_e32 v27, 2, v27
	v_mov_b32_e32 v64, 0
	v_mul_f32_e32 v68, v62, v66
	v_lshlrev_b32_e32 v31, 7, v103
	v_lshlrev_b32_e32 v42, 7, v102
	v_bitop3_b32 v37, v34, v37, s16 bitop3:0x6c
	v_bitop3_b32 v41, v34, v41, s16 bitop3:0x6c
	v_bitop3_b32 v34, v34, v26, s16 bitop3:0x4e
	v_xad_u32 v56, v55, v53, s41
	v_xad_u32 v59, v57, v53, s41
	v_xad_u32 v65, v60, v53, s41
	v_xad_u32 v53, v39, v53, s41
	v_xad_u32 v55, v55, v40, s41
	v_xad_u32 v57, v57, v40, s41
	v_xad_u32 v60, v60, v40, s41
	v_xad_u32 v39, v39, v40, s41
	v_xad_u32 v38, v35, v38, 0
	v_xad_u32 v40, v35, v50, 0
	v_xad_u32 v35, v35, v52, 0
	v_bitop3_b32 v0, v0, s16, v27 bitop3:0xc8
	s_movk_i32 s0, 0x4000
	s_mov_b32 s40, 0
	v_add_u32_e32 v106, s41, v29
	v_mov_b32_e32 v76, v68
	v_mov_b32_e32 v77, v68
	v_mov_b32_e32 v78, v66
	v_mov_b32_e32 v79, v66
	v_mov_b32_e32 v63, v62
	v_mov_b32_e32 v83, v82
	v_or_b32_e32 v109, v28, v34
	v_or_b32_e32 v110, v28, v41
	v_or_b32_e32 v111, v28, v37
	v_or3_b32 v112, v28, v0, v26
	v_add3_u32 v113, v108, v29, s0
	v_add3_u32 v114, v107, v29, s0
	v_add_u32_e32 v115, v51, v42
	v_add_u32_e32 v116, v46, v42
	v_add_u32_e32 v117, v48, v42
	v_add_u32_e32 v118, v43, v42
	v_add_u32_e32 v119, v33, v31
	v_add_u32_e32 v120, v32, v31
	v_add_u32_e32 v121, v38, v30
	v_add_u32_e32 v122, v40, v30
	v_add_u32_e32 v123, v35, v30
	v_add_u32_e32 v124, v56, v54
	v_add_u32_e32 v125, v59, v58
	v_add_u32_e32 v126, v65, v61
	v_add_u32_e32 v127, v53, v67
	v_add_u32_e32 v128, v55, v54
	v_add_u32_e32 v129, v57, v58
	v_add_u32_e32 v130, v60, v61
	v_add_u32_e32 v131, v39, v67
	v_add_u32_e32 v132, v45, v42
	v_add_u32_e32 v133, v47, v42
	v_add_u32_e32 v134, v49, v42
	v_add_u32_e32 v135, v44, v42
	v_mov_b32_e32 v65, v64
	v_mov_b32_e32 v86, v64
	v_mov_b32_e32 v87, v64
	v_mov_b32_e32 v88, v64
	v_mov_b32_e32 v89, v64
	v_mov_b32_e32 v90, v64
	v_mov_b32_e32 v91, v64
	global_load_dwordx4 v[156:159], v[80:81], off
	global_load_dwordx4 v[160:163], v[80:81], off offset:64
	global_load_dwordx4 v[164:167], v[80:81], off offset:128
	global_load_dwordx4 v[168:171], v[80:81], off offset:192

.LBB0_842:
	v_add_u32_e32 v59, 0, v0
	ds_read_b128 v[50:53], v59
	ds_read_b128 v[136:139], v59 offset:2048
	v_add_u32_e32 v59, 0, v54
	ds_read_b128 v[140:143], v59
	ds_read_b128 v[144:147], v59 offset:2048
	s_add_i32 s0, s13, 1
	s_waitcnt lgkmcnt(3)
	v_mfma_f32_16x16x32_bf16 v[50:53], v[50:53], v[46:49], 0
	s_cmp_lt_u32 s13, s96
	s_cselect_b64 s[48:49], -1, 0
	s_cmp_lt_u32 s0, s96
	s_waitcnt lgkmcnt(1)
	v_mfma_f32_16x16x32_bf16 v[50:53], v[140:143], v[42:45], v[50:53]
	s_cselect_b64 s[50:51], -1, 0
	s_cmp_eq_u32 s96, s13
	s_cselect_b64 s[64:65], -1, 0
	s_cmp_eq_u32 s86, s13
	s_cselect_b64 s[84:85], -1, 0
	s_and_b64 s[0:1], s[64:65], s[28:29]
	s_or_b64 vcc, s[48:49], s[0:1]
	s_and_b64 s[40:41], s[64:65], s[30:31]
	s_or_b64 s[40:41], s[48:49], s[40:41]
	v_cndmask_b32_e32 v50, 0, v50, vcc
	v_mfma_f32_16x16x32_bf16 v[136:139], v[136:139], v[46:49], 0
	v_bfe_u32 v59, v50, 16, 1
	v_cndmask_b32_e64 v51, 0, v51, s[40:41]
	s_and_b64 s[44:45], s[64:65], s[34:35]
	v_add3_u32 v50, v50, v59, s39
	v_bfe_u32 v59, v51, 16, 1
	s_or_b64 s[44:45], s[48:49], s[44:45]
	v_lshrrev_b32_e32 v50, 16, v50
	v_add3_u32 v51, v51, v59, s39
	s_and_b64 s[64:65], s[64:65], s[36:37]
	v_and_or_b32 v50, v51, s38, v50
	v_cndmask_b32_e64 v51, 0, v52, s[44:45]
	s_waitcnt lgkmcnt(0)
	v_mfma_f32_16x16x32_bf16 v[136:139], v[144:147], v[42:45], v[136:139]
	s_or_b64 s[48:49], s[48:49], s[64:65]
	v_bfe_u32 v52, v51, 16, 1
	v_add3_u32 v51, v51, v52, s39
	v_cndmask_b32_e64 v52, 0, v53, s[48:49]
	s_and_b64 s[0:1], s[84:85], s[28:29]
	v_bfe_u32 v53, v52, 16, 1
	s_or_b64 s[0:1], s[50:51], s[0:1]
	v_lshrrev_b32_e32 v51, 16, v51
	v_add3_u32 v52, v52, v53, s39
	s_and_b64 s[42:43], s[84:85], s[30:31]
	v_and_or_b32 v51, v52, s38, v51
	v_cndmask_b32_e64 v52, 0, v136, s[0:1]
	s_or_b64 s[42:43], s[50:51], s[42:43]
	v_bfe_u32 v53, v52, 16, 1
	v_add3_u32 v52, v52, v53, s39
	v_cndmask_b32_e64 v53, 0, v137, s[42:43]
	s_and_b64 s[46:47], s[84:85], s[34:35]
	v_bfe_u32 v59, v53, 16, 1
	s_or_b64 s[46:47], s[50:51], s[46:47]
	v_lshrrev_b32_e32 v52, 16, v52
	v_add3_u32 v53, v53, v59, s39
	s_and_b64 s[64:65], s[84:85], s[36:37]
	v_and_or_b32 v52, v53, s38, v52
	v_cndmask_b32_e64 v53, 0, v138, s[46:47]
	s_or_b64 s[50:51], s[50:51], s[64:65]
	v_bfe_u32 v59, v53, 16, 1
	v_add3_u32 v53, v53, v59, s39
	v_cndmask_b32_e64 v59, 0, v139, s[50:51]
	v_bfe_u32 v60, v59, 16, 1
	v_lshrrev_b32_e32 v53, 16, v53
	v_add3_u32 v59, v59, v60, s39
	v_and_or_b32 v53, v59, s38, v53
	v_add_u32_e32 v59, 0, v55
	ds_read_b64_tr_b16 v[136:137], v59 offset:49152
	ds_read_b64_tr_b16 v[138:139], v59 offset:51200
	v_add_u32_e32 v59, 0, v56
	s_waitcnt lgkmcnt(0)
	v_mfma_f32_16x16x32_bf16 v[38:41], v[136:139], v[50:53], v[38:41]
	ds_read_b64_tr_b16 v[136:137], v59 offset:49152
	ds_read_b64_tr_b16 v[138:139], v59 offset:51200
	v_add_u32_e32 v59, 0, v57
	s_add_i32 s13, s13, 2
	s_waitcnt lgkmcnt(0)
	v_mfma_f32_16x16x32_bf16 v[34:37], v[136:139], v[50:53], v[34:37]
	ds_read_b64_tr_b16 v[136:137], v59 offset:49152
	ds_read_b64_tr_b16 v[138:139], v59 offset:51200
	v_add_u32_e32 v59, 0, v58
	v_add_u32_e32 v58, 0x1000, v58
	s_waitcnt lgkmcnt(0)
	v_mfma_f32_16x16x32_bf16 v[30:33], v[136:139], v[50:53], v[30:33]
	ds_read_b64_tr_b16 v[136:137], v59 offset:49152
	ds_read_b64_tr_b16 v[138:139], v59 offset:51200
	v_add_u32_e32 v57, 0x1000, v57
	v_add_u32_e32 v56, 0x1000, v56
	s_waitcnt lgkmcnt(0)
	v_mfma_f32_16x16x32_bf16 v[26:29], v[136:139], v[50:53], v[26:29]
	v_add_u32_e32 v55, 0x1000, v55
	v_add_u32_e32 v54, 0x1000, v54
	v_add_u32_e32 v0, 0x1000, v0
	s_cmp_eq_u32 s79, s13
	s_cbranch_scc0 .LBB0_842
	v_add_u32_e32 v0, v106, v107
	ds_read_b128 v[50:53], v0
	v_add_u32_e32 v67, v106, v108
	ds_read_b128 v[54:57], v67
	v_mov_b32_e32 v69, v68
	s_mov_b64 s[0:1], 0x13c00600
	s_cmp_eq_u32 s12, 32
	s_mov_b32 s40, s12
	s_waitcnt lgkmcnt(1)
	v_mfma_f32_16x16x32_bf16 v[50:53], v[50:53], v[46:49], 0
	ds_read_b128 v[136:139], v67 offset:4096
	s_waitcnt lgkmcnt(1)
	v_mfma_f32_16x16x32_bf16 v[58:61], v[54:57], v[42:45], v[50:53]
	ds_read_b128 v[54:57], v67 offset:2048
	s_nop 3
	ds_read_b128 v[50:53], v0 offset:2048
	s_waitcnt lgkmcnt(0)
	v_mfma_f32_16x16x32_bf16 v[50:53], v[50:53], v[46:49], 0
	v_mfma_f32_16x16x32_bf16 v[54:57], v[54:57], v[42:45], v[50:53]
	s_nop 6
	ds_read_b128 v[50:53], v0 offset:4096
	s_waitcnt lgkmcnt(0)
	v_mfma_f32_16x16x32_bf16 v[50:53], v[50:53], v[46:49], 0
	v_mfma_f32_16x16x32_bf16 v[50:53], v[136:139], v[42:45], v[50:53]
	ds_read_b128 v[136:139], v0 offset:6144
	s_waitcnt lgkmcnt(0)
	v_mfma_f32_16x16x32_bf16 v[46:49], v[136:139], v[46:49], 0
	ds_read_b128 v[136:139], v67 offset:6144
	v_mov_b32_e32 v67, v66
	s_waitcnt lgkmcnt(0)
	v_mfma_f32_16x16x32_bf16 v[42:45], v[136:139], v[42:45], v[46:49]
	s_nop 3
	ds_read_b64_tr_b16 v[46:47], v121 offset:49152
	ds_read_b64_tr_b16 v[48:49], v121 offset:51200
	ds_read_b64_tr_b16 v[136:137], v122 offset:32768
	ds_read_b64_tr_b16 v[138:139], v122 offset:34816
	ds_read_b64_tr_b16 v[140:141], v121 offset:53248
	ds_read_b64_tr_b16 v[142:143], v121 offset:55296
	ds_read_b64_tr_b16 v[144:145], v122 offset:36864
	ds_read_b64_tr_b16 v[146:147], v122 offset:38912
	s_waitcnt lgkmcnt(4)
	v_mfma_f32_16x16x32_bf16 v[136:139], v[46:49], v[136:139], 0
	s_waitcnt lgkmcnt(0)
	v_mfma_f32_16x16x32_bf16 v[136:139], v[140:143], v[144:147], v[136:139]
	ds_read_b64_tr_b16 v[144:145], v121 offset:57344
	ds_read_b64_tr_b16 v[146:147], v121 offset:59392
	ds_read_b64_tr_b16 v[148:149], v122 offset:40960
	ds_read_b64_tr_b16 v[150:151], v122 offset:43008
	s_waitcnt lgkmcnt(0)
	v_mfma_f32_16x16x32_bf16 v[136:139], v[144:147], v[148:151], v[136:139]
	ds_read_b64_tr_b16 v[148:149], v121 offset:61440
	ds_read_b64_tr_b16 v[150:151], v121 offset:63488
	ds_read_b64_tr_b16 v[152:153], v122 offset:45056
	ds_read_b64_tr_b16 v[154:155], v122 offset:47104
	s_waitcnt lgkmcnt(0)
	v_mfma_f32_16x16x32_bf16 v[136:139], v[148:151], v[152:155], v[136:139]
	s_nop 7
	v_pk_mul_f32 v[138:139], v[66:67], v[138:139]
	v_pk_mul_f32 v[136:137], v[78:79], v[136:137]
	v_pk_fma_f32 v[86:87], v[68:69], v[86:87], v[138:139]
	v_pk_fma_f32 v[64:65], v[76:77], v[64:65], v[136:137]
	ds_read_b64_tr_b16 v[136:137], v123 offset:32768
	ds_read_b64_tr_b16 v[138:139], v123 offset:34816
	s_waitcnt lgkmcnt(0)
	v_mfma_f32_16x16x32_bf16 v[46:49], v[46:49], v[136:139], 0
	ds_read_b64_tr_b16 v[136:137], v123 offset:36864
	ds_read_b64_tr_b16 v[138:139], v123 offset:38912
	v_bfe_u32 v0, v64, 16, 1
	v_add3_u32 v0, v64, v0, s39
	s_waitcnt lgkmcnt(0)
	v_mfma_f32_16x16x32_bf16 v[46:49], v[140:143], v[136:139], v[46:49]
	ds_read_b64_tr_b16 v[136:137], v123 offset:40960
	ds_read_b64_tr_b16 v[138:139], v123 offset:43008
	s_waitcnt lgkmcnt(0)
	v_mfma_f32_16x16x32_bf16 v[46:49], v[144:147], v[136:139], v[46:49]
	ds_read_b64_tr_b16 v[136:137], v123 offset:45056
	ds_read_b64_tr_b16 v[138:139], v123 offset:47104
	s_waitcnt lgkmcnt(0)
	s_barrier
	v_mfma_f32_16x16x32_bf16 v[46:49], v[148:151], v[136:139], v[46:49]
	v_mov_b32_e32 v137, v40
	v_mov_b32_e32 v40, v39
	v_mov_b32_e32 v136, v38
	s_nop 4
	v_pk_mul_f32 v[46:47], v[78:79], v[46:47]
	v_pk_mul_f32 v[48:49], v[66:67], v[48:49]
	v_pk_fma_f32 v[88:89], v[76:77], v[88:89], v[46:47]
	v_lshlrev_b64 v[46:47], 11, v[100:101]
	v_mov_b32_e32 v101, v60
	v_mov_b32_e32 v60, v59
	s_waitcnt vmcnt(3)
	v_and_b32_e32 v67, 0xffff0000, v98
	v_mov_b32_e32 v100, v58
	v_pk_fma_f32 v[58:59], v[62:63], v[60:61], v[40:41]
	v_lshlrev_b32_e32 v41, 16, v99
	v_lshlrev_b32_e32 v60, 16, v98
	v_mul_f32_e32 v39, 0xbfb8aa3b, v67
	v_mul_f32_e32 v38, 0xbfb8aa3b, v60
	v_exp_f32_e32 v40, v39
	v_mul_f32_e32 v39, 0xbfb8aa3b, v41
	v_exp_f32_e32 v38, v38
	v_exp_f32_e32 v39, v39
	v_lshl_add_u64 v[46:47], s[60:61], 0, v[46:47]
	v_lshl_add_u64 v[46:47], s[68:69], 1, v[46:47]
	v_pk_fma_f32 v[90:91], v[68:69], v[90:91], v[48:49]
	v_lshl_add_u64 v[48:49], v[74:75], 1, v[46:47]
	v_pk_add_f32 v[38:39], v[38:39], 1.0 op_sel_hi:[1,0]
	v_lshl_add_u64 v[46:47], v[48:49], 0, s[0:1]
	v_div_scale_f32 v69, s[0:1], v39, v39, v41
	v_rcp_f32_e32 v98, v69
	v_and_b32_e32 v61, 0xffff0000, v99
	v_pk_fma_f32 v[100:101], v[62:63], v[100:101], v[136:137]
	v_fma_f32 v99, -v69, v98, 1.0
	v_fmac_f32_e32 v98, v99, v98
	v_div_scale_f32 v99, vcc, v41, v39, v41
	v_mul_f32_e32 v136, v99, v98
	v_fma_f32 v137, -v69, v136, v99
	v_fmac_f32_e32 v136, v137, v98
	v_fma_f32 v69, -v69, v136, v99
	v_div_fmas_f32 v69, v69, v98, v136
	v_div_fixup_f32 v39, v69, v39, v41
	v_div_scale_f32 v41, s[0:1], v38, v38, v60
	v_rcp_f32_e32 v69, v41
	ds_write_b16_d16_hi v124, v0
	v_bfe_u32 v0, v65, 16, 1
	v_add3_u32 v0, v65, v0, s39
	v_fma_f32 v98, -v41, v69, 1.0
	v_fmac_f32_e32 v69, v98, v69
	v_div_scale_f32 v98, vcc, v60, v38, v60
	v_mul_f32_e32 v99, v98, v69
	v_fma_f32 v136, -v41, v99, v98
	v_fmac_f32_e32 v99, v136, v69
	v_fma_f32 v41, -v41, v99, v98
	v_div_fmas_f32 v41, v41, v69, v99
	v_div_fixup_f32 v38, v41, v38, v60
	v_mul_f32_e32 v41, 0xbfb8aa3b, v61
	v_exp_f32_e32 v41, v41
	ds_write_b16_d16_hi v125, v0
	v_bfe_u32 v0, v86, 16, 1
	v_add3_u32 v0, v86, v0, s39
	v_pk_add_f32 v[40:41], v[40:41], 1.0 op_sel_hi:[1,0]
	ds_write_b16_d16_hi v126, v0
	v_div_scale_f32 v60, s[0:1], v41, v41, v61
	v_rcp_f32_e32 v69, v60
	v_bfe_u32 v0, v87, 16, 1
	v_add3_u32 v0, v87, v0, s39
	ds_write_b16_d16_hi v127, v0
	v_fma_f32 v98, -v60, v69, 1.0
	v_fmac_f32_e32 v69, v98, v69
	v_div_scale_f32 v98, vcc, v61, v41, v61
	v_mul_f32_e32 v99, v98, v69
	v_fma_f32 v136, -v60, v99, v98
	v_fmac_f32_e32 v99, v136, v69
	v_fma_f32 v60, -v60, v99, v98
	v_div_fmas_f32 v60, v60, v69, v99
	v_div_fixup_f32 v41, v60, v41, v61
	v_div_scale_f32 v60, s[0:1], v40, v40, v67
	v_rcp_f32_e32 v61, v60
	v_bfe_u32 v0, v88, 16, 1
	v_add3_u32 v0, v88, v0, s39
	ds_write_b16_d16_hi v128, v0
	v_fma_f32 v69, -v60, v61, 1.0
	v_fmac_f32_e32 v61, v69, v61
	v_div_scale_f32 v69, vcc, v67, v40, v67
	v_mul_f32_e32 v98, v69, v61
	v_fma_f32 v99, -v60, v98, v69
	v_fmac_f32_e32 v98, v99, v61
	v_fma_f32 v60, -v60, v98, v69
	v_div_fmas_f32 v60, v60, v61, v98
	v_div_fixup_f32 v40, v60, v40, v67
	v_mov_b32_e32 v61, v56
	v_mov_b32_e32 v99, v36
	v_mov_b32_e32 v56, v55
	v_mov_b32_e32 v36, v35
	s_waitcnt vmcnt(2)
	v_and_b32_e32 v67, 0xffff0000, v96
	v_mov_b32_e32 v60, v54
	v_pk_fma_f32 v[54:55], v[62:63], v[56:57], v[36:37]
	v_lshlrev_b32_e32 v37, 16, v97
	v_lshlrev_b32_e32 v56, 16, v96
	v_mul_f32_e32 v35, 0xbfb8aa3b, v67
	v_mov_b32_e32 v98, v34
	v_mul_f32_e32 v34, 0xbfb8aa3b, v56
	v_exp_f32_e32 v36, v35
	v_mul_f32_e32 v35, 0xbfb8aa3b, v37
	v_exp_f32_e32 v34, v34
	v_exp_f32_e32 v35, v35
	v_and_b32_e32 v57, 0xffff0000, v97
	v_pk_fma_f32 v[60:61], v[62:63], v[60:61], v[98:99]
	v_bfe_u32 v0, v89, 16, 1
	v_pk_add_f32 v[34:35], v[34:35], 1.0 op_sel_hi:[1,0]
	v_add3_u32 v0, v89, v0, s39
	v_div_scale_f32 v69, s[0:1], v35, v35, v37
	v_rcp_f32_e32 v96, v69
	ds_write_b16_d16_hi v129, v0
	v_bfe_u32 v0, v90, 16, 1
	v_add3_u32 v0, v90, v0, s39
	v_fma_f32 v97, -v69, v96, 1.0
	v_fmac_f32_e32 v96, v97, v96
	v_div_scale_f32 v97, vcc, v37, v35, v37
	v_mul_f32_e32 v98, v97, v96
	v_fma_f32 v99, -v69, v98, v97
	v_fmac_f32_e32 v98, v99, v96
	v_fma_f32 v69, -v69, v98, v97
	v_div_fmas_f32 v69, v69, v96, v98
	v_div_fixup_f32 v35, v69, v35, v37
	v_div_scale_f32 v37, s[0:1], v34, v34, v56
	v_rcp_f32_e32 v69, v37
	ds_write_b16_d16_hi v130, v0
	v_bfe_u32 v0, v91, 16, 1
	v_add3_u32 v0, v91, v0, s39
	v_fma_f32 v96, -v37, v69, 1.0
	v_fmac_f32_e32 v69, v96, v69
	v_div_scale_f32 v96, vcc, v56, v34, v56
	v_mul_f32_e32 v97, v96, v69
	v_fma_f32 v98, -v37, v97, v96
	v_fmac_f32_e32 v97, v98, v69
	v_fma_f32 v37, -v37, v97, v96
	v_div_fmas_f32 v37, v37, v69, v97
	v_div_fixup_f32 v34, v37, v34, v56
	v_mul_f32_e32 v37, 0xbfb8aa3b, v57
	v_exp_f32_e32 v37, v37
	ds_write_b16_d16_hi v131, v0
	v_add_f32_e32 v0, 0, v100
	v_add_f32_e32 v0, v58, v0
	v_pk_add_f32 v[36:37], v[36:37], 1.0 op_sel_hi:[1,0]
	v_add_f32_e32 v0, v101, v0
	v_div_scale_f32 v56, s[0:1], v37, v37, v57
	v_rcp_f32_e32 v69, v56
	v_add_f32_e32 v0, v59, v0
	v_add_f32_e32 v0, v0, v60
	v_add_f32_e32 v0, v54, v0
	v_fma_f32 v96, -v56, v69, 1.0
	v_fmac_f32_e32 v69, v96, v69
	v_div_scale_f32 v96, vcc, v57, v37, v57
	v_mul_f32_e32 v97, v96, v69
	v_fma_f32 v98, -v56, v97, v96
	v_fmac_f32_e32 v97, v98, v69
	v_fma_f32 v56, -v56, v97, v96
	v_div_fmas_f32 v56, v56, v69, v97
	v_div_fixup_f32 v37, v56, v37, v57
	v_div_scale_f32 v56, s[0:1], v36, v36, v67
	v_rcp_f32_e32 v57, v56
	v_add_f32_e32 v0, v61, v0
	v_add_f32_e32 v0, v55, v0
	v_fma_f32 v69, -v56, v57, 1.0
	v_fmac_f32_e32 v57, v69, v57
	v_div_scale_f32 v69, vcc, v67, v36, v67
	v_mul_f32_e32 v96, v69, v57
	v_fma_f32 v97, -v56, v96, v69
	v_fmac_f32_e32 v96, v97, v57
	v_fma_f32 v56, -v56, v96, v69
	v_div_fmas_f32 v56, v56, v57, v96
	v_div_fixup_f32 v36, v56, v36, v67
	v_mov_b32_e32 v56, v50
	v_mov_b32_e32 v57, v52
	v_mov_b32_e32 v96, v30
	v_mov_b32_e32 v97, v32
	v_pk_fma_f32 v[96:97], v[62:63], v[56:57], v[96:97]
	v_mov_b32_e32 v52, v51
	v_mov_b32_e32 v32, v31
	s_waitcnt vmcnt(1)
	v_and_b32_e32 v56, 0xffff0000, v94
	v_pk_fma_f32 v[50:51], v[62:63], v[52:53], v[32:33]
	v_lshlrev_b32_e32 v33, 16, v95
	v_lshlrev_b32_e32 v52, 16, v94
	v_mul_f32_e32 v31, 0xbfb8aa3b, v56
	v_mul_f32_e32 v30, 0xbfb8aa3b, v52
	v_exp_f32_e32 v32, v31
	v_mul_f32_e32 v31, 0xbfb8aa3b, v33
	v_exp_f32_e32 v30, v30
	v_exp_f32_e32 v31, v31
	v_and_b32_e32 v53, 0xffff0000, v95
	v_add_f32_e32 v0, v0, v96
	v_add_f32_e32 v0, v50, v0
	v_pk_add_f32 v[30:31], v[30:31], 1.0 op_sel_hi:[1,0]
	v_add_f32_e32 v0, v97, v0
	v_div_scale_f32 v57, s[0:1], v31, v31, v33
	v_rcp_f32_e32 v67, v57
	v_add_f32_e32 v0, v51, v0
	v_fma_f32 v69, -v57, v67, 1.0
	v_fmac_f32_e32 v67, v69, v67
	v_div_scale_f32 v69, vcc, v33, v31, v33
	v_mul_f32_e32 v94, v69, v67
	v_fma_f32 v95, -v57, v94, v69
	v_fmac_f32_e32 v94, v95, v67
	v_fma_f32 v57, -v57, v94, v69
	v_div_fmas_f32 v57, v57, v67, v94
	v_div_fixup_f32 v31, v57, v31, v33
	v_div_scale_f32 v33, s[0:1], v30, v30, v52
	v_rcp_f32_e32 v57, v33
	s_nop 0
	v_fma_f32 v67, -v33, v57, 1.0
	v_fmac_f32_e32 v57, v67, v57
	v_div_scale_f32 v67, vcc, v52, v30, v52
	v_mul_f32_e32 v69, v67, v57
	v_fma_f32 v94, -v33, v69, v67
	v_fmac_f32_e32 v69, v94, v57
	v_fma_f32 v33, -v33, v69, v67
	v_div_fmas_f32 v33, v33, v57, v69
	v_div_fixup_f32 v30, v33, v30, v52
	v_mul_f32_e32 v33, 0xbfb8aa3b, v53
	v_exp_f32_e32 v33, v33
	s_nop 0
	v_pk_add_f32 v[32:33], v[32:33], 1.0 op_sel_hi:[1,0]
	s_nop 0
	v_div_scale_f32 v52, s[0:1], v33, v33, v53
	v_rcp_f32_e32 v57, v52
	s_nop 0
	v_fma_f32 v67, -v52, v57, 1.0
	v_fmac_f32_e32 v57, v67, v57
	v_div_scale_f32 v67, vcc, v53, v33, v53
	v_mul_f32_e32 v69, v67, v57
	v_fma_f32 v94, -v52, v69, v67
	v_fmac_f32_e32 v69, v94, v57
	v_fma_f32 v52, -v52, v69, v67
	v_div_fmas_f32 v52, v52, v57, v69
	v_div_fixup_f32 v33, v52, v33, v53
	v_div_scale_f32 v52, s[0:1], v32, v32, v56
	v_rcp_f32_e32 v53, v52
	s_nop 0
	v_fma_f32 v57, -v52, v53, 1.0
	v_fmac_f32_e32 v53, v57, v53
	v_div_scale_f32 v57, vcc, v56, v32, v56
	v_mul_f32_e32 v67, v57, v53
	v_fma_f32 v69, -v52, v67, v57
	v_fmac_f32_e32 v67, v69, v53
	v_fma_f32 v52, -v52, v67, v57
	v_div_fmas_f32 v52, v52, v53, v67
	v_div_fixup_f32 v32, v52, v32, v56
	v_mov_b32_e32 v52, v42
	v_mov_b32_e32 v53, v44
	v_mov_b32_e32 v56, v26
	v_mov_b32_e32 v57, v28
	v_pk_fma_f32 v[98:99], v[62:63], v[52:53], v[56:57]
	v_mov_b32_e32 v44, v43
	v_mov_b32_e32 v28, v27
	v_pk_fma_f32 v[26:27], v[62:63], v[44:45], v[28:29]
	v_add_f32_e32 v0, v0, v98
	v_add_f32_e32 v0, v26, v0
	v_add_f32_e32 v0, v99, v0
	v_add_f32_e32 v0, v27, v0
	v_mov_b32_e32 v28, v0
	s_nop 1
	v_permlane16_swap_b32_e32 v0, v28
	v_add_f32_e32 v0, v0, v28
	v_mov_b32_e32 v28, v0
	s_nop 1
	v_permlane32_swap_b32_e32 v0, v28
	v_add_f32_e32 v0, v0, v28
	v_mul_f32_e32 v0, 0x3c800000, v0
	v_pk_add_f32 v[58:59], v[58:59], v[0:1] op_sel_hi:[1,0] neg_lo:[0,1] neg_hi:[0,1]
	v_pk_add_f32 v[94:95], v[100:101], v[0:1] op_sel_hi:[1,0] neg_lo:[0,1] neg_hi:[0,1]
	v_pk_mul_f32 v[28:29], v[58:59], v[58:59]
	v_mul_f32_e32 v44, v95, v95
	v_pk_fma_f32 v[42:43], v[94:95], v[94:95], v[28:29]
	v_pk_add_f32 v[56:57], v[60:61], v[0:1] op_sel_hi:[1,0] neg_lo:[0,1] neg_hi:[0,1]
	v_pk_add_f32 v[42:43], v[44:45], v[42:43] op_sel_hi:[0,1]
	v_pk_add_f32 v[28:29], v[28:29], v[42:43] op_sel:[1,0] op_sel_hi:[0,1]
	v_pk_fma_f32 v[28:29], v[56:57], v[56:57], v[28:29]
	v_pk_add_f32 v[54:55], v[54:55], v[0:1] op_sel_hi:[1,0] neg_lo:[0,1] neg_hi:[0,1]
	v_mul_f32_e32 v42, v57, v57
	v_pk_fma_f32 v[28:29], v[54:55], v[54:55], v[28:29]
	v_pk_add_f32 v[52:53], v[96:97], v[0:1] op_sel_hi:[1,0] neg_lo:[0,1] neg_hi:[0,1]
	v_pk_add_f32 v[28:29], v[42:43], v[28:29] op_sel_hi:[0,1]
	v_mul_f32_e32 v42, v55, v55
	v_pk_add_f32 v[28:29], v[42:43], v[28:29] op_sel_hi:[0,1]
	v_pk_fma_f32 v[28:29], v[52:53], v[52:53], v[28:29]
	v_pk_add_f32 v[50:51], v[50:51], v[0:1] op_sel_hi:[1,0] neg_lo:[0,1] neg_hi:[0,1]
	v_mul_f32_e32 v42, v53, v53
	v_pk_fma_f32 v[28:29], v[50:51], v[50:51], v[28:29]
	v_pk_add_f32 v[44:45], v[98:99], v[0:1] op_sel_hi:[1,0] neg_lo:[0,1] neg_hi:[0,1]
	v_pk_add_f32 v[28:29], v[42:43], v[28:29] op_sel_hi:[0,1]
	v_mul_f32_e32 v42, v51, v51
	v_pk_add_f32 v[28:29], v[42:43], v[28:29] op_sel_hi:[0,1]
	v_pk_fma_f32 v[28:29], v[44:45], v[44:45], v[28:29]
	v_pk_add_f32 v[42:43], v[26:27], v[0:1] op_sel_hi:[1,0] neg_lo:[0,1] neg_hi:[0,1]
	v_mul_f32_e32 v0, v45, v45
	v_pk_fma_f32 v[26:27], v[42:43], v[42:43], v[28:29]
	v_pk_mul_f32 v[38:39], v[38:39], v[94:95]
	v_pk_add_f32 v[26:27], v[0:1], v[26:27] op_sel_hi:[0,1]
	v_mul_f32_e32 v0, v43, v43
	v_pk_add_f32 v[26:27], v[0:1], v[26:27] op_sel_hi:[0,1]
	v_mov_b32_e32 v0, v26
	v_pk_mul_f32 v[40:41], v[40:41], v[58:59]
	s_nop 0
	v_permlane16_swap_b32_e32 v26, v0
	v_add_f32_e32 v0, v26, v0
	v_mov_b32_e32 v26, v0
	v_pk_mul_f32 v[34:35], v[34:35], v[56:57]
	s_nop 0
	v_permlane32_swap_b32_e32 v0, v26
	v_add_f32_e32 v0, v0, v26
	v_fmamk_f32 v0, v0, 0x3c800000, v250
	v_cmp_gt_f32_e32 vcc, s78, v0
	v_mul_f32_e32 v26, 0x4f800000, v0
	v_pk_mul_f32 v[36:37], v[36:37], v[54:55]
	v_cndmask_b32_e32 v0, v0, v26, vcc
	v_sqrt_f32_e32 v26, v0
	v_pk_mul_f32 v[30:31], v[30:31], v[52:53]
	v_pk_mul_f32 v[32:33], v[32:33], v[50:51]
	v_add_u32_e32 v27, -1, v26
	v_fma_f32 v28, -v27, v26, v0
	v_cmp_ge_f32_e64 s[0:1], 0, v28
	v_add_u32_e32 v28, 1, v26
	s_nop 0
	v_cndmask_b32_e64 v27, v26, v27, s[0:1]
	v_fma_f32 v26, -v28, v26, v0
	v_cmp_lt_f32_e64 s[0:1], 0, v26
	s_nop 1
	v_cndmask_b32_e64 v26, v27, v28, s[0:1]
	v_mul_f32_e32 v27, 0x37800000, v26
	v_cndmask_b32_e32 v26, v26, v27, vcc
	v_cmp_class_f32_e32 vcc, v0, v231
	s_nop 1
	v_cndmask_b32_e32 v0, v26, v0, vcc
	v_div_scale_f32 v26, s[0:1], v0, v0, 1.0
	v_rcp_f32_e32 v27, v26
	s_mov_b32 s0, 0x13c00000
	v_fma_f32 v28, -v26, v27, 1.0
	v_fmac_f32_e32 v27, v28, v27
	v_div_scale_f32 v28, vcc, 1.0, v0, 1.0
	v_mul_f32_e32 v29, v28, v27
	v_fma_f32 v60, -v26, v29, v28
	v_fmac_f32_e32 v29, v60, v27
	v_fma_f32 v26, -v26, v29, v28
	v_div_fmas_f32 v26, v26, v27, v29
	v_div_fixup_f32 v0, v26, v0, 1.0
	s_nop 1
	v_mov_b64_e32 v[26:27], v[156:157]
	v_mov_b64_e32 v[28:29], v[158:159]
	v_pk_mul_f32 v[38:39], v[38:39], v[0:1] op_sel_hi:[1,0]
	v_pk_mul_f32 v[40:41], v[40:41], v[0:1] op_sel_hi:[1,0]
	v_pk_mul_f32 v[34:35], v[34:35], v[0:1] op_sel_hi:[1,0]
	v_pk_mul_f32 v[36:37], v[36:37], v[0:1] op_sel_hi:[1,0]
	v_pk_mul_f32 v[30:31], v[30:31], v[0:1] op_sel_hi:[1,0]
	v_pk_mul_f32 v[32:33], v[32:33], v[0:1] op_sel_hi:[1,0]
	s_waitcnt vmcnt(0)
	v_mov_b32_e32 v60, v26
	v_mov_b32_e32 v61, v28
	v_pk_mul_f32 v[38:39], v[60:61], v[38:39]
	v_mov_b32_e32 v28, v27
	v_pk_mul_f32 v[26:27], v[28:29], v[40:41]
	v_and_b32_sdwa v29, v38, v220 dst_sel:DWORD dst_unused:UNUSED_PAD src0_sel:WORD_1 src1_sel:DWORD
	v_and_b32_sdwa v28, v39, v220 dst_sel:DWORD dst_unused:UNUSED_PAD src0_sel:WORD_1 src1_sel:DWORD
	v_add3_u32 v29, v38, v29, s39
	v_and_b32_sdwa v38, v27, v220 dst_sel:DWORD dst_unused:UNUSED_PAD src0_sel:WORD_1 src1_sel:DWORD
	v_add3_u32 v28, v39, v28, s39
	v_and_b32_sdwa v39, v26, v220 dst_sel:DWORD dst_unused:UNUSED_PAD src0_sel:WORD_1 src1_sel:DWORD
	v_add3_u32 v27, v27, v38, s39
	v_add3_u32 v26, v26, v39, s39
	v_and_b32_e32 v27, 0xffff0000, v27
	v_and_b32_e32 v26, 0xffff0000, v26
	v_or_b32_sdwa v27, v27, v28 dst_sel:DWORD dst_unused:UNUSED_PAD src0_sel:DWORD src1_sel:WORD_1
	v_add_co_u32_e32 v28, vcc, s0, v48
	v_or_b32_sdwa v26, v26, v29 dst_sel:DWORD dst_unused:UNUSED_PAD src0_sel:DWORD src1_sel:WORD_1
	s_nop 0
	v_addc_co_u32_e32 v29, vcc, 0, v49, vcc
	global_store_dwordx2 v[28:29], v[26:27], off offset:1536
	s_nop 1
	v_mov_b64_e32 v[26:27], v[160:161]
	v_mov_b64_e32 v[28:29], v[162:163]
	v_mov_b32_e32 v38, v26
	v_mov_b32_e32 v39, v28
	v_pk_mul_f32 v[34:35], v[38:39], v[34:35]
	v_mov_b32_e32 v28, v27
	v_pk_mul_f32 v[26:27], v[28:29], v[36:37]
	v_and_b32_sdwa v28, v35, v220 dst_sel:DWORD dst_unused:UNUSED_PAD src0_sel:WORD_1 src1_sel:DWORD
	v_and_b32_sdwa v29, v34, v220 dst_sel:DWORD dst_unused:UNUSED_PAD src0_sel:WORD_1 src1_sel:DWORD
	v_add3_u32 v29, v34, v29, s39
	v_add3_u32 v28, v35, v28, s39
	v_and_b32_sdwa v34, v27, v220 dst_sel:DWORD dst_unused:UNUSED_PAD src0_sel:WORD_1 src1_sel:DWORD
	v_and_b32_sdwa v35, v26, v220 dst_sel:DWORD dst_unused:UNUSED_PAD src0_sel:WORD_1 src1_sel:DWORD
	v_add3_u32 v27, v27, v34, s39
	v_add3_u32 v26, v26, v35, s39
	v_and_b32_e32 v27, 0xffff0000, v27
	v_and_b32_e32 v26, 0xffff0000, v26
	v_or_b32_sdwa v27, v27, v28 dst_sel:DWORD dst_unused:UNUSED_PAD src0_sel:DWORD src1_sel:WORD_1
	v_or_b32_sdwa v26, v26, v29 dst_sel:DWORD dst_unused:UNUSED_PAD src0_sel:DWORD src1_sel:WORD_1
	global_store_dwordx2 v[46:47], v[26:27], off offset:32
	s_nop 1
	v_mov_b64_e32 v[26:27], v[164:165]
	v_mov_b64_e32 v[28:29], v[166:167]
	v_and_b32_e32 v37, 0xffff0000, v92
	v_and_b32_e32 v36, 0xffff0000, v93
	v_mov_b32_e32 v34, v26
	v_mov_b32_e32 v35, v28
	v_pk_mul_f32 v[30:31], v[34:35], v[30:31]
	v_mov_b32_e32 v28, v27
	v_pk_mul_f32 v[26:27], v[28:29], v[32:33]
	v_and_b32_sdwa v28, v31, v220 dst_sel:DWORD dst_unused:UNUSED_PAD src0_sel:WORD_1 src1_sel:DWORD
	v_and_b32_sdwa v29, v30, v220 dst_sel:DWORD dst_unused:UNUSED_PAD src0_sel:WORD_1 src1_sel:DWORD
	v_add3_u32 v29, v30, v29, s39
	v_add3_u32 v28, v31, v28, s39
	v_and_b32_sdwa v30, v27, v220 dst_sel:DWORD dst_unused:UNUSED_PAD src0_sel:WORD_1 src1_sel:DWORD
	v_and_b32_sdwa v31, v26, v220 dst_sel:DWORD dst_unused:UNUSED_PAD src0_sel:WORD_1 src1_sel:DWORD
	v_add3_u32 v27, v27, v30, s39
	v_add3_u32 v26, v26, v31, s39
	v_and_b32_e32 v27, 0xffff0000, v27
	v_and_b32_e32 v26, 0xffff0000, v26
	v_or_b32_sdwa v27, v27, v28 dst_sel:DWORD dst_unused:UNUSED_PAD src0_sel:DWORD src1_sel:WORD_1
	v_or_b32_sdwa v26, v26, v29 dst_sel:DWORD dst_unused:UNUSED_PAD src0_sel:DWORD src1_sel:WORD_1
	global_store_dwordx2 v[46:47], v[26:27], off offset:64
	s_nop 1
	v_mov_b64_e32 v[26:27], v[168:169]
	v_mov_b64_e32 v[28:29], v[170:171]
	v_lshlrev_b32_e32 v33, 16, v93
	v_lshlrev_b32_e32 v34, 16, v92
	v_mul_f32_e32 v31, 0xbfb8aa3b, v37
	v_mul_f32_e32 v30, 0xbfb8aa3b, v34
	v_exp_f32_e32 v32, v31
	v_mul_f32_e32 v31, 0xbfb8aa3b, v33
	v_exp_f32_e32 v30, v30
	v_exp_f32_e32 v31, v31
	s_nop 0
	v_pk_add_f32 v[30:31], v[30:31], 1.0 op_sel_hi:[1,0]
	s_nop 0
	v_div_scale_f32 v35, s[0:1], v31, v31, v33
	v_rcp_f32_e32 v38, v35
	s_nop 0
	v_fma_f32 v39, -v35, v38, 1.0
	v_fmac_f32_e32 v38, v39, v38
	v_div_scale_f32 v39, vcc, v33, v31, v33
	v_mul_f32_e32 v40, v39, v38
	v_fma_f32 v41, -v35, v40, v39
	v_fmac_f32_e32 v40, v41, v38
	v_fma_f32 v35, -v35, v40, v39
	v_div_fmas_f32 v35, v35, v38, v40
	v_div_fixup_f32 v31, v35, v31, v33
	v_div_scale_f32 v33, s[0:1], v30, v30, v34
	v_rcp_f32_e32 v35, v33
	s_nop 0
	v_fma_f32 v38, -v33, v35, 1.0
	v_fmac_f32_e32 v35, v38, v35
	v_div_scale_f32 v38, vcc, v34, v30, v34
	v_mul_f32_e32 v39, v38, v35
	v_fma_f32 v40, -v33, v39, v38
	v_fmac_f32_e32 v39, v40, v35
	v_fma_f32 v33, -v33, v39, v38
	v_div_fmas_f32 v33, v33, v35, v39
	v_div_fixup_f32 v30, v33, v30, v34
	v_pk_mul_f32 v[30:31], v[30:31], v[44:45]
	v_mov_b32_e32 v34, v26
	v_mul_f32_e32 v26, 0xbfb8aa3b, v36
	v_exp_f32_e32 v33, v26
	v_mov_b32_e32 v35, v28
	v_pk_mul_f32 v[30:31], v[30:31], v[0:1] op_sel_hi:[1,0]
	v_pk_add_f32 v[32:33], v[32:33], 1.0 op_sel_hi:[1,0]
	s_nop 0
	v_div_scale_f32 v26, s[0:1], v33, v33, v36
	v_rcp_f32_e32 v28, v26
	v_pk_mul_f32 v[30:31], v[34:35], v[30:31]
	v_fma_f32 v34, -v26, v28, 1.0
	v_fmac_f32_e32 v28, v34, v28
	v_div_scale_f32 v34, vcc, v36, v33, v36
	v_mul_f32_e32 v35, v34, v28
	v_fma_f32 v38, -v26, v35, v34
	v_fmac_f32_e32 v35, v38, v28
	v_fma_f32 v26, -v26, v35, v34
	v_div_fmas_f32 v26, v26, v28, v35
	v_div_fixup_f32 v33, v26, v33, v36
	v_div_scale_f32 v26, s[0:1], v32, v32, v37
	v_rcp_f32_e32 v28, v26
	s_nop 0
	v_fma_f32 v34, -v26, v28, 1.0
	v_fmac_f32_e32 v28, v34, v28
	v_div_scale_f32 v34, vcc, v37, v32, v37
	v_mul_f32_e32 v35, v34, v28
	v_fma_f32 v36, -v26, v35, v34
	v_fmac_f32_e32 v35, v36, v28
	v_fma_f32 v26, -v26, v35, v34
	v_div_fmas_f32 v26, v26, v28, v35
	v_div_fixup_f32 v32, v26, v32, v37
	v_pk_mul_f32 v[32:33], v[32:33], v[42:43]
	v_mov_b32_e32 v28, v27
	v_pk_mul_f32 v[32:33], v[32:33], v[0:1] op_sel_hi:[1,0]
	v_and_b32_sdwa v0, v31, v220 dst_sel:DWORD dst_unused:UNUSED_PAD src0_sel:WORD_1 src1_sel:DWORD
	v_pk_mul_f32 v[26:27], v[28:29], v[32:33]
	v_and_b32_sdwa v28, v30, v220 dst_sel:DWORD dst_unused:UNUSED_PAD src0_sel:WORD_1 src1_sel:DWORD
	v_add3_u32 v28, v30, v28, s39
	v_and_b32_sdwa v29, v27, v220 dst_sel:DWORD dst_unused:UNUSED_PAD src0_sel:WORD_1 src1_sel:DWORD
	v_and_b32_sdwa v30, v26, v220 dst_sel:DWORD dst_unused:UNUSED_PAD src0_sel:WORD_1 src1_sel:DWORD
	v_add3_u32 v27, v27, v29, s39
	v_add3_u32 v26, v26, v30, s39
	v_add3_u32 v0, v31, v0, s39
	v_and_b32_e32 v27, 0xffff0000, v27
	v_and_b32_e32 v26, 0xffff0000, v26
	v_or_b32_sdwa v27, v27, v0 dst_sel:DWORD dst_unused:UNUSED_PAD src0_sel:DWORD src1_sel:WORD_1
	v_or_b32_sdwa v26, v26, v28 dst_sel:DWORD dst_unused:UNUSED_PAD src0_sel:DWORD src1_sel:WORD_1
	global_store_dwordx2 v[46:47], v[26:27], off offset:96
	s_cbranch_scc0 .LBB0_835
	s_waitcnt lgkmcnt(0)
	s_barrier
